# E29: E25 + G1 K-loop heavy memory phases reordered: the 6 LDS-DMA issues go before the 8 ds_read_b128 (to see whether DMA issue behind LDS reads is the phase bottleneck)
# speedup vs baseline: 1.0041x; 1.0041x over previous
.LBB0_1213:
	s_add_u32 s35, s42, 0x100
	s_addc_u32 s37, s43, 0
	s_mov_b32 s39, -2
	s_mov_b64 s[42:43], 0
	ds_read_b128 v[70:73], v190
	ds_read_b128 v[74:77], v190 offset:1024
	ds_read_b128 v[78:81], v190 offset:2048
	ds_read_b128 v[82:85], v190 offset:3072
	ds_read_b128 v[94:97], v191
	ds_read_b128 v[98:101], v191 offset:1024
	ds_read_b128 v[102:105], v191 offset:2048
	ds_read_b128 v[106:109], v191 offset:3072
	s_add_u32 s44, s42, 0x100
	s_addc_u32 s45, s43, 0
	s_add_u32 s48, s35, s42
	s_addc_u32 s49, s37, s43
	s_cmp_eq_u32 s39, 12
	s_cselect_b64 vcc, -1, 0
	s_and_b64 s[46:47], vcc, exec
	s_cselect_b32 s73, 0, s44
	s_cselect_b32 s72, 0, s45
	s_cselect_b32 s46, s0, s48
	s_cselect_b32 s47, s1, s49
	s_add_u32 s48, s14, s73
	s_addc_u32 s49, s15, s72
	s_add_i32 m0, s11, 0xc000
	s_add_u32 s42, s24, s42
	s_addc_u32 s43, s25, s43
	ds_read_b128 v[176:179], v192
	ds_read_b128 v[180:183], v192 offset:1024
	ds_read_b128 v[194:197], v192 offset:2048
	ds_read_b128 v[198:201], v192 offset:3072
	ds_read_b128 v[202:205], v192 offset:4096
	ds_read_b128 v[206:209], v192 offset:5120
	ds_read_b128 v[210:213], v192 offset:6144
	ds_read_b128 v[214:217], v192 offset:7168
	global_load_lds_dwordx4 v187, s[42:43]
	s_add_i32 m0, s11, 0xe000
	v_mov_b32_e32 v0, v172
	global_load_lds_dwordx4 v186, s[42:43]
	v_mov_b32_e32 v169, v173
	v_lshlrev_b32_e32 v184, 11, v0
	v_lshlrev_b32_e32 v185, 11, v169
	v_bfe_u32 v0, v0, 16, 16
	v_bfe_u32 v169, v169, 16, 16
	v_and_b32_e32 v184, 0x7fff800, v184
	v_and_b32_e32 v185, 0x7fff800, v185
	v_lshl_add_u32 v0, v0, 11, v175
	v_lshl_add_u32 v169, v169, 11, v175
	v_add_u32_e32 v184, v184, v175
	v_add_u32_e32 v185, v185, v175
	v_cndmask_b32_e32 v168, v168, v0, vcc
	v_cndmask_b32_e32 v186, v186, v169, vcc
	v_cndmask_b32_e32 v170, v170, v184, vcc
	v_cndmask_b32_e32 v187, v187, v185, vcc
	s_waitcnt vmcnt(24)
	s_waitcnt lgkmcnt(0)
	s_barrier
	s_setprio 1
	s_waitcnt lgkmcnt(0)
	v_mfma_i32_16x16x64_i8 v[158:161], v[70:73], v[176:179], 0
	v_mfma_i32_16x16x64_i8 v[150:153], v[78:81], v[176:179], 0
	v_mfma_i32_16x16x64_i8 v[142:145], v[70:73], v[194:197], 0
	v_mfma_i32_16x16x64_i8 v[134:137], v[78:81], v[194:197], 0
	v_mfma_i32_16x16x64_i8 v[126:129], v[70:73], v[202:205], 0
	v_mfma_i32_16x16x64_i8 v[118:121], v[78:81], v[202:205], 0
	v_mfma_i32_16x16x64_i8 v[110:113], v[70:73], v[210:213], 0
	v_mfma_i32_16x16x64_i8 v[86:89], v[78:81], v[210:213], 0
	v_mfma_i32_16x16x64_i8 v[158:161], v[74:77], v[180:183], v[158:161]
	v_mfma_i32_16x16x64_i8 v[150:153], v[82:85], v[180:183], v[150:153]
	v_mfma_i32_16x16x64_i8 v[142:145], v[74:77], v[198:201], v[142:145]
	v_mfma_i32_16x16x64_i8 v[134:137], v[82:85], v[198:201], v[134:137]
	v_mfma_i32_16x16x64_i8 v[126:129], v[74:77], v[206:209], v[126:129]
	v_mfma_i32_16x16x64_i8 v[118:121], v[82:85], v[206:209], v[118:121]
	v_mfma_i32_16x16x64_i8 v[110:113], v[74:77], v[214:217], v[110:113]
	v_mfma_i32_16x16x64_i8 v[86:89], v[82:85], v[214:217], v[86:89]
	s_setprio 0
	s_setprio 1
	v_mfma_i32_16x16x64_i8 v[154:157], v[94:97], v[176:179], 0
	v_mfma_i32_16x16x64_i8 v[146:149], v[102:105], v[176:179], 0
	v_mfma_i32_16x16x64_i8 v[138:141], v[94:97], v[194:197], 0
	v_mfma_i32_16x16x64_i8 v[130:133], v[102:105], v[194:197], 0
	v_mfma_i32_16x16x64_i8 v[122:125], v[94:97], v[202:205], 0
	v_mfma_i32_16x16x64_i8 v[114:117], v[102:105], v[202:205], 0
	v_mfma_i32_16x16x64_i8 v[90:93], v[94:97], v[210:213], 0
	v_mfma_i32_16x16x64_i8 v[66:69], v[102:105], v[210:213], 0
	v_mfma_i32_16x16x64_i8 v[154:157], v[98:101], v[180:183], v[154:157]
	v_mfma_i32_16x16x64_i8 v[146:149], v[106:109], v[180:183], v[146:149]
	v_mfma_i32_16x16x64_i8 v[138:141], v[98:101], v[198:201], v[138:141]
	v_mfma_i32_16x16x64_i8 v[130:133], v[106:109], v[198:201], v[130:133]
	v_mfma_i32_16x16x64_i8 v[122:125], v[98:101], v[206:209], v[122:125]
	v_mfma_i32_16x16x64_i8 v[114:117], v[106:109], v[206:209], v[114:117]
	v_mfma_i32_16x16x64_i8 v[90:93], v[98:101], v[214:217], v[90:93]
	v_mfma_i32_16x16x64_i8 v[66:69], v[106:109], v[214:217], v[66:69]
	s_setprio 0
	s_barrier
	s_add_i32 s42, s67, s57
	v_lshl_add_u64 v[184:185], s[46:47], 0, v[164:165]
	s_mov_b32 m0, s42
	s_nop 0
	global_load_lds_dwordx4 v[184:185], off
	s_add_i32 m0, s42, 0x2000
	s_add_u32 s42, s46, 0x40000
	v_lshl_add_u64 v[218:219], s[46:47], 0, v[166:167]
	s_addc_u32 s43, s47, 0
	s_add_i32 s72, s68, s57
	global_load_lds_dwordx4 v[218:219], off
	v_lshl_add_u64 v[220:221], s[42:43], 0, v[164:165]
	s_mov_b32 m0, s72
	v_mov_b32_e32 v169, v171
	global_load_lds_dwordx4 v[220:221], off
	v_lshl_add_u64 v[220:221], s[42:43], 0, v[166:167]
	s_add_i32 m0, s72, 0x2000
	v_lshl_add_u64 v[222:223], s[48:49], 0, v[168:169]
	global_load_lds_dwordx4 v[220:221], off
	s_mov_b32 m0, s11
	v_lshl_add_u64 v[220:221], s[48:49], 0, v[170:171]
	global_load_lds_dwordx4 v170, s[48:49]
	s_mov_b32 m0, s58
	s_nop 0
	global_load_lds_dwordx4 v168, s[48:49]
	ds_read_b128 v[176:179], v192 offset:16384
	ds_read_b128 v[180:183], v192 offset:17408
	ds_read_b128 v[194:197], v192 offset:18432
	ds_read_b128 v[198:201], v192 offset:19456
	ds_read_b128 v[202:205], v192 offset:20480
	ds_read_b128 v[206:209], v192 offset:21504
	ds_read_b128 v[210:213], v192 offset:22528
	ds_read_b128 v[214:217], v192 offset:23552
	s_waitcnt vmcnt(8)
	s_waitcnt lgkmcnt(0)
	s_barrier
	s_setprio 1
	s_waitcnt lgkmcnt(0)
	v_mfma_i32_16x16x64_i8 v[62:65], v[70:73], v[176:179], 0
	v_mfma_i32_16x16x64_i8 v[54:57], v[78:81], v[176:179], 0
	v_mfma_i32_16x16x64_i8 v[46:49], v[70:73], v[194:197], 0
	v_mfma_i32_16x16x64_i8 v[38:41], v[78:81], v[194:197], 0
	v_mfma_i32_16x16x64_i8 v[30:33], v[70:73], v[202:205], 0
	v_mfma_i32_16x16x64_i8 v[22:25], v[78:81], v[202:205], 0
	v_mfma_i32_16x16x64_i8 v[14:17], v[70:73], v[210:213], 0
	v_mfma_i32_16x16x64_i8 v[6:9], v[78:81], v[210:213], 0
	v_mfma_i32_16x16x64_i8 v[62:65], v[74:77], v[180:183], v[62:65]
	v_mfma_i32_16x16x64_i8 v[54:57], v[82:85], v[180:183], v[54:57]
	v_mfma_i32_16x16x64_i8 v[46:49], v[74:77], v[198:201], v[46:49]
	v_mfma_i32_16x16x64_i8 v[38:41], v[82:85], v[198:201], v[38:41]
	v_mfma_i32_16x16x64_i8 v[30:33], v[74:77], v[206:209], v[30:33]
	v_mfma_i32_16x16x64_i8 v[22:25], v[82:85], v[206:209], v[22:25]
	v_mfma_i32_16x16x64_i8 v[14:17], v[74:77], v[214:217], v[14:17]
	v_mfma_i32_16x16x64_i8 v[6:9], v[82:85], v[214:217], v[6:9]
	s_setprio 0
	s_setprio 1
	v_mfma_i32_16x16x64_i8 v[58:61], v[94:97], v[176:179], 0
	v_mfma_i32_16x16x64_i8 v[50:53], v[102:105], v[176:179], 0
	v_mfma_i32_16x16x64_i8 v[42:45], v[94:97], v[194:197], 0
	v_mfma_i32_16x16x64_i8 v[34:37], v[102:105], v[194:197], 0
	v_mfma_i32_16x16x64_i8 v[26:29], v[94:97], v[202:205], 0
	v_mfma_i32_16x16x64_i8 v[18:21], v[102:105], v[202:205], 0
	v_mfma_i32_16x16x64_i8 v[10:13], v[94:97], v[210:213], 0
	v_mfma_i32_16x16x64_i8 v[2:5], v[102:105], v[210:213], 0
	v_mfma_i32_16x16x64_i8 v[58:61], v[98:101], v[180:183], v[58:61]
	v_mfma_i32_16x16x64_i8 v[50:53], v[106:109], v[180:183], v[50:53]
	v_mfma_i32_16x16x64_i8 v[42:45], v[98:101], v[198:201], v[42:45]
	v_mfma_i32_16x16x64_i8 v[34:37], v[106:109], v[198:201], v[34:37]
	v_mfma_i32_16x16x64_i8 v[26:29], v[98:101], v[206:209], v[26:29]
	v_mfma_i32_16x16x64_i8 v[18:21], v[106:109], v[206:209], v[18:21]
	v_mfma_i32_16x16x64_i8 v[10:13], v[98:101], v[214:217], v[10:13]
	v_mfma_i32_16x16x64_i8 v[2:5], v[106:109], v[214:217], v[2:5]
	s_setprio 0
	s_barrier
	s_add_i32 s42, 0, 0x18000
	v_add_u32_e32 v0, s42, v189
	s_add_i32 s72, 0, 0x1c000
	ds_read_b128 v[70:73], v0
	ds_read_b128 v[74:77], v0 offset:1024
	ds_read_b128 v[78:81], v0 offset:2048
	ds_read_b128 v[82:85], v0 offset:3072
	v_add_u32_e32 v0, s72, v189
	ds_read_b128 v[94:97], v0
	ds_read_b128 v[98:101], v0 offset:1024
	ds_read_b128 v[102:105], v0 offset:2048
	ds_read_b128 v[106:109], v0 offset:3072
	s_mov_b32 m0, s59
	ds_read_b128 v[176:179], v192 offset:32768
	ds_read_b128 v[180:183], v192 offset:33792
	ds_read_b128 v[194:197], v192 offset:34816
	ds_read_b128 v[198:201], v192 offset:35840
	ds_read_b128 v[202:205], v192 offset:36864
	ds_read_b128 v[206:209], v192 offset:37888
	ds_read_b128 v[210:213], v192 offset:38912
	ds_read_b128 v[214:217], v192 offset:39936
	global_load_lds_dwordx4 v187, s[48:49]
	s_mov_b32 m0, s60
	s_nop 0
	global_load_lds_dwordx4 v186, s[48:49]
	s_waitcnt vmcnt(8)
	s_waitcnt lgkmcnt(0)
	s_barrier
	s_setprio 1
	s_waitcnt lgkmcnt(0)
	v_mfma_i32_16x16x64_i8 v[158:161], v[70:73], v[176:179], v[158:161]
	v_mfma_i32_16x16x64_i8 v[150:153], v[78:81], v[176:179], v[150:153]
	v_mfma_i32_16x16x64_i8 v[142:145], v[70:73], v[194:197], v[142:145]
	v_mfma_i32_16x16x64_i8 v[134:137], v[78:81], v[194:197], v[134:137]
	v_mfma_i32_16x16x64_i8 v[126:129], v[70:73], v[202:205], v[126:129]
	v_mfma_i32_16x16x64_i8 v[118:121], v[78:81], v[202:205], v[118:121]
	v_mfma_i32_16x16x64_i8 v[110:113], v[70:73], v[210:213], v[110:113]
	v_mfma_i32_16x16x64_i8 v[86:89], v[78:81], v[210:213], v[86:89]
	v_mfma_i32_16x16x64_i8 v[158:161], v[74:77], v[180:183], v[158:161]
	v_mfma_i32_16x16x64_i8 v[150:153], v[82:85], v[180:183], v[150:153]
	v_mfma_i32_16x16x64_i8 v[142:145], v[74:77], v[198:201], v[142:145]
	v_mfma_i32_16x16x64_i8 v[134:137], v[82:85], v[198:201], v[134:137]
	v_mfma_i32_16x16x64_i8 v[126:129], v[74:77], v[206:209], v[126:129]
	v_mfma_i32_16x16x64_i8 v[118:121], v[82:85], v[206:209], v[118:121]
	v_mfma_i32_16x16x64_i8 v[110:113], v[74:77], v[214:217], v[110:113]
	v_mfma_i32_16x16x64_i8 v[86:89], v[82:85], v[214:217], v[86:89]
	s_setprio 0
	s_setprio 1
	v_mfma_i32_16x16x64_i8 v[154:157], v[94:97], v[176:179], v[154:157]
	v_mfma_i32_16x16x64_i8 v[146:149], v[102:105], v[176:179], v[146:149]
	v_mfma_i32_16x16x64_i8 v[138:141], v[94:97], v[194:197], v[138:141]
	v_mfma_i32_16x16x64_i8 v[130:133], v[102:105], v[194:197], v[130:133]
	v_mfma_i32_16x16x64_i8 v[122:125], v[94:97], v[202:205], v[122:125]
	v_mfma_i32_16x16x64_i8 v[114:117], v[102:105], v[202:205], v[114:117]
	v_mfma_i32_16x16x64_i8 v[90:93], v[94:97], v[210:213], v[90:93]
	v_mfma_i32_16x16x64_i8 v[66:69], v[102:105], v[210:213], v[66:69]
	v_mfma_i32_16x16x64_i8 v[154:157], v[98:101], v[180:183], v[154:157]
	v_mfma_i32_16x16x64_i8 v[146:149], v[106:109], v[180:183], v[146:149]
	v_mfma_i32_16x16x64_i8 v[138:141], v[98:101], v[198:201], v[138:141]
	v_mfma_i32_16x16x64_i8 v[130:133], v[106:109], v[198:201], v[130:133]
	v_mfma_i32_16x16x64_i8 v[122:125], v[98:101], v[206:209], v[122:125]
	v_mfma_i32_16x16x64_i8 v[114:117], v[106:109], v[206:209], v[114:117]
	v_mfma_i32_16x16x64_i8 v[90:93], v[98:101], v[214:217], v[90:93]
	v_mfma_i32_16x16x64_i8 v[66:69], v[106:109], v[214:217], v[66:69]
	s_setprio 0
	s_barrier
	s_add_i32 s42, s42, s57
	v_lshl_add_u64 v[184:185], v[184:185], 0, s[22:23]
	s_mov_b32 m0, s42
	s_nop 0
	global_load_lds_dwordx4 v[184:185], off
	s_add_i32 m0, s42, 0x2000
	s_add_u32 s42, s46, 0x40080
	v_lshl_add_u64 v[184:185], v[218:219], 0, s[22:23]
	s_addc_u32 s43, s47, 0
	s_add_i32 s46, s72, s57
	global_load_lds_dwordx4 v[184:185], off
	v_lshl_add_u64 v[184:185], s[42:43], 0, v[164:165]
	s_mov_b32 m0, s46
	s_nop 0
	global_load_lds_dwordx4 v[184:185], off
	v_lshl_add_u64 v[184:185], s[42:43], 0, v[166:167]
	s_add_i32 m0, s46, 0x2000
	s_nop 0
	global_load_lds_dwordx4 v[184:185], off
	v_lshl_add_u64 v[184:185], v[220:221], 0, s[22:23]
	s_mov_b32 m0, s63
	s_nop 0
	global_load_lds_dwordx4 v[184:185], off
	v_lshl_add_u64 v[184:185], v[222:223], 0, s[22:23]
	s_mov_b32 m0, s64
	s_nop 0
	global_load_lds_dwordx4 v[184:185], off
	ds_read_b128 v[176:179], v192 offset:49152
	ds_read_b128 v[180:183], v192 offset:50176
	ds_read_b128 v[194:197], v192 offset:51200
	ds_read_b128 v[198:201], v192 offset:52224
	ds_read_b128 v[202:205], v192 offset:53248
	ds_read_b128 v[206:209], v192 offset:54272
	ds_read_b128 v[210:213], v192 offset:55296
	ds_read_b128 v[214:217], v192 offset:56320
	s_waitcnt vmcnt(8)
	s_waitcnt lgkmcnt(0)
	s_barrier
	s_setprio 1
	s_waitcnt lgkmcnt(0)
	v_mfma_i32_16x16x64_i8 v[62:65], v[70:73], v[176:179], v[62:65]
	v_mfma_i32_16x16x64_i8 v[54:57], v[78:81], v[176:179], v[54:57]
	v_mfma_i32_16x16x64_i8 v[46:49], v[70:73], v[194:197], v[46:49]
	v_mfma_i32_16x16x64_i8 v[38:41], v[78:81], v[194:197], v[38:41]
	v_mfma_i32_16x16x64_i8 v[30:33], v[70:73], v[202:205], v[30:33]
	v_mfma_i32_16x16x64_i8 v[22:25], v[78:81], v[202:205], v[22:25]
	v_mfma_i32_16x16x64_i8 v[14:17], v[70:73], v[210:213], v[14:17]
	v_mfma_i32_16x16x64_i8 v[6:9], v[78:81], v[210:213], v[6:9]
	v_mfma_i32_16x16x64_i8 v[62:65], v[74:77], v[180:183], v[62:65]
	v_mfma_i32_16x16x64_i8 v[54:57], v[82:85], v[180:183], v[54:57]
	v_mfma_i32_16x16x64_i8 v[46:49], v[74:77], v[198:201], v[46:49]
	v_mfma_i32_16x16x64_i8 v[38:41], v[82:85], v[198:201], v[38:41]
	v_mfma_i32_16x16x64_i8 v[30:33], v[74:77], v[206:209], v[30:33]
	v_mfma_i32_16x16x64_i8 v[22:25], v[82:85], v[206:209], v[22:25]
	v_mfma_i32_16x16x64_i8 v[14:17], v[74:77], v[214:217], v[14:17]
	v_mfma_i32_16x16x64_i8 v[6:9], v[82:85], v[214:217], v[6:9]
	s_setprio 0
	s_setprio 1
	v_mfma_i32_16x16x64_i8 v[58:61], v[94:97], v[176:179], v[58:61]
	v_mfma_i32_16x16x64_i8 v[50:53], v[102:105], v[176:179], v[50:53]
	v_mfma_i32_16x16x64_i8 v[42:45], v[94:97], v[194:197], v[42:45]
	v_mfma_i32_16x16x64_i8 v[34:37], v[102:105], v[194:197], v[34:37]
	v_mfma_i32_16x16x64_i8 v[26:29], v[94:97], v[202:205], v[26:29]
	v_mfma_i32_16x16x64_i8 v[18:21], v[102:105], v[202:205], v[18:21]
	v_mfma_i32_16x16x64_i8 v[10:13], v[94:97], v[210:213], v[10:13]
	v_mfma_i32_16x16x64_i8 v[2:5], v[102:105], v[210:213], v[2:5]
	v_mfma_i32_16x16x64_i8 v[58:61], v[98:101], v[180:183], v[58:61]
	v_mfma_i32_16x16x64_i8 v[50:53], v[106:109], v[180:183], v[50:53]
	v_mfma_i32_16x16x64_i8 v[42:45], v[98:101], v[198:201], v[42:45]
	v_mfma_i32_16x16x64_i8 v[34:37], v[106:109], v[198:201], v[34:37]
	v_mfma_i32_16x16x64_i8 v[26:29], v[98:101], v[206:209], v[26:29]
	v_mfma_i32_16x16x64_i8 v[18:21], v[106:109], v[206:209], v[18:21]
	v_mfma_i32_16x16x64_i8 v[10:13], v[98:101], v[214:217], v[10:13]
	v_mfma_i32_16x16x64_i8 v[2:5], v[106:109], v[214:217], v[2:5]
	s_setprio 0
	s_barrier
	s_add_i32 s39, s39, 2
	s_cmp_gt_u32 s39, 13
	s_mov_b64 s[42:43], s[44:45]
	s_cbranch_scc0 .LBB0_1214
	s_branch .Lkexit_1214
	s_nop 0
	s_nop 0
	s_nop 0
	s_nop 0
	s_nop 0
	s_nop 0
	s_nop 0
	s_nop 0
	s_nop 0
	s_nop 0
	s_nop 0
	s_nop 0
	s_nop 0
	s_nop 0
	s_nop 0
	s_nop 0
	s_nop 0
	s_nop 0
	s_nop 0
	s_nop 0
	s_nop 0
	s_nop 0
	s_nop 0
	s_nop 0
	s_nop 0
	s_nop 0
	s_nop 0
	s_nop 0
	s_nop 0
	s_nop 0
	s_nop 0
.LBB0_1214:
	ds_read_b128 v[70:73], v190
	ds_read_b128 v[74:77], v190 offset:1024
	ds_read_b128 v[78:81], v190 offset:2048
	ds_read_b128 v[82:85], v190 offset:3072
	ds_read_b128 v[94:97], v191
	ds_read_b128 v[98:101], v191 offset:1024
	ds_read_b128 v[102:105], v191 offset:2048
	ds_read_b128 v[106:109], v191 offset:3072
	s_add_u32 s44, s42, 0x100
	s_addc_u32 s45, s43, 0
	s_add_u32 s48, s35, s42
	s_addc_u32 s49, s37, s43
	s_cmp_eq_u32 s39, 12
	s_cselect_b64 vcc, -1, 0
	s_and_b64 s[46:47], vcc, exec
	s_cselect_b32 s73, 0, s44
	s_cselect_b32 s72, 0, s45
	s_cselect_b32 s46, s0, s48
	s_cselect_b32 s47, s1, s49
	s_add_u32 s48, s14, s73
	s_addc_u32 s49, s15, s72
	s_add_i32 m0, s11, 0xc000
	s_add_u32 s42, s24, s42
	s_addc_u32 s43, s25, s43
	ds_read_b128 v[176:179], v192
	ds_read_b128 v[180:183], v192 offset:1024
	ds_read_b128 v[194:197], v192 offset:2048
	ds_read_b128 v[198:201], v192 offset:3072
	ds_read_b128 v[202:205], v192 offset:4096
	ds_read_b128 v[206:209], v192 offset:5120
	ds_read_b128 v[210:213], v192 offset:6144
	ds_read_b128 v[214:217], v192 offset:7168
	global_load_lds_dwordx4 v187, s[42:43]
	s_add_i32 m0, s11, 0xe000
	v_mov_b32_e32 v0, v172
	global_load_lds_dwordx4 v186, s[42:43]
	v_mov_b32_e32 v169, v173
	v_lshlrev_b32_e32 v184, 11, v0
	v_lshlrev_b32_e32 v185, 11, v169
	v_bfe_u32 v0, v0, 16, 16
	v_bfe_u32 v169, v169, 16, 16
	v_and_b32_e32 v184, 0x7fff800, v184
	v_and_b32_e32 v185, 0x7fff800, v185
	v_lshl_add_u32 v0, v0, 11, v175
	v_lshl_add_u32 v169, v169, 11, v175
	v_add_u32_e32 v184, v184, v175
	v_add_u32_e32 v185, v185, v175
	v_cndmask_b32_e32 v168, v168, v0, vcc
	v_cndmask_b32_e32 v186, v186, v169, vcc
	v_cndmask_b32_e32 v170, v170, v184, vcc
	v_cndmask_b32_e32 v187, v187, v185, vcc
	s_waitcnt vmcnt(8)
	s_waitcnt lgkmcnt(0)
	s_barrier
	s_setprio 1
	s_waitcnt lgkmcnt(0)
	v_mfma_i32_16x16x64_i8 v[158:161], v[70:73], v[176:179], v[158:161]
	v_mfma_i32_16x16x64_i8 v[150:153], v[78:81], v[176:179], v[150:153]
	v_mfma_i32_16x16x64_i8 v[142:145], v[70:73], v[194:197], v[142:145]
	v_mfma_i32_16x16x64_i8 v[134:137], v[78:81], v[194:197], v[134:137]
	v_mfma_i32_16x16x64_i8 v[126:129], v[70:73], v[202:205], v[126:129]
	v_mfma_i32_16x16x64_i8 v[118:121], v[78:81], v[202:205], v[118:121]
	v_mfma_i32_16x16x64_i8 v[110:113], v[70:73], v[210:213], v[110:113]
	v_mfma_i32_16x16x64_i8 v[86:89], v[78:81], v[210:213], v[86:89]
	v_mfma_i32_16x16x64_i8 v[158:161], v[74:77], v[180:183], v[158:161]
	v_mfma_i32_16x16x64_i8 v[150:153], v[82:85], v[180:183], v[150:153]
	v_mfma_i32_16x16x64_i8 v[142:145], v[74:77], v[198:201], v[142:145]
	v_mfma_i32_16x16x64_i8 v[134:137], v[82:85], v[198:201], v[134:137]
	v_mfma_i32_16x16x64_i8 v[126:129], v[74:77], v[206:209], v[126:129]
	v_mfma_i32_16x16x64_i8 v[118:121], v[82:85], v[206:209], v[118:121]
	v_mfma_i32_16x16x64_i8 v[110:113], v[74:77], v[214:217], v[110:113]
	v_mfma_i32_16x16x64_i8 v[86:89], v[82:85], v[214:217], v[86:89]
	s_setprio 0
	s_setprio 1
	v_mfma_i32_16x16x64_i8 v[154:157], v[94:97], v[176:179], v[154:157]
	v_mfma_i32_16x16x64_i8 v[146:149], v[102:105], v[176:179], v[146:149]
	v_mfma_i32_16x16x64_i8 v[138:141], v[94:97], v[194:197], v[138:141]
	v_mfma_i32_16x16x64_i8 v[130:133], v[102:105], v[194:197], v[130:133]
	v_mfma_i32_16x16x64_i8 v[122:125], v[94:97], v[202:205], v[122:125]
	v_mfma_i32_16x16x64_i8 v[114:117], v[102:105], v[202:205], v[114:117]
	v_mfma_i32_16x16x64_i8 v[90:93], v[94:97], v[210:213], v[90:93]
	v_mfma_i32_16x16x64_i8 v[66:69], v[102:105], v[210:213], v[66:69]
	v_mfma_i32_16x16x64_i8 v[154:157], v[98:101], v[180:183], v[154:157]
	v_mfma_i32_16x16x64_i8 v[146:149], v[106:109], v[180:183], v[146:149]
	v_mfma_i32_16x16x64_i8 v[138:141], v[98:101], v[198:201], v[138:141]
	v_mfma_i32_16x16x64_i8 v[130:133], v[106:109], v[198:201], v[130:133]
	v_mfma_i32_16x16x64_i8 v[122:125], v[98:101], v[206:209], v[122:125]
	v_mfma_i32_16x16x64_i8 v[114:117], v[106:109], v[206:209], v[114:117]
	v_mfma_i32_16x16x64_i8 v[90:93], v[98:101], v[214:217], v[90:93]
	v_mfma_i32_16x16x64_i8 v[66:69], v[106:109], v[214:217], v[66:69]
	s_setprio 0
	s_barrier
	s_add_i32 s42, s67, s57
	v_lshl_add_u64 v[184:185], s[46:47], 0, v[164:165]
	s_mov_b32 m0, s42
	s_nop 0
	global_load_lds_dwordx4 v[184:185], off
	s_add_i32 m0, s42, 0x2000
	s_add_u32 s42, s46, 0x40000
	v_lshl_add_u64 v[218:219], s[46:47], 0, v[166:167]
	s_addc_u32 s43, s47, 0
	s_add_i32 s72, s68, s57
	global_load_lds_dwordx4 v[218:219], off
	v_lshl_add_u64 v[220:221], s[42:43], 0, v[164:165]
	s_mov_b32 m0, s72
	v_mov_b32_e32 v169, v171
	global_load_lds_dwordx4 v[220:221], off
	v_lshl_add_u64 v[220:221], s[42:43], 0, v[166:167]
	s_add_i32 m0, s72, 0x2000
	v_lshl_add_u64 v[222:223], s[48:49], 0, v[168:169]
	global_load_lds_dwordx4 v[220:221], off
	s_mov_b32 m0, s11
	v_lshl_add_u64 v[220:221], s[48:49], 0, v[170:171]
	global_load_lds_dwordx4 v170, s[48:49]
	s_mov_b32 m0, s58
	s_nop 0
	global_load_lds_dwordx4 v168, s[48:49]
	ds_read_b128 v[176:179], v192 offset:16384
	ds_read_b128 v[180:183], v192 offset:17408
	ds_read_b128 v[194:197], v192 offset:18432
	ds_read_b128 v[198:201], v192 offset:19456
	ds_read_b128 v[202:205], v192 offset:20480
	ds_read_b128 v[206:209], v192 offset:21504
	ds_read_b128 v[210:213], v192 offset:22528
	ds_read_b128 v[214:217], v192 offset:23552
	s_waitcnt vmcnt(8)
	s_waitcnt lgkmcnt(0)
	s_barrier
	s_setprio 1
	s_waitcnt lgkmcnt(0)
	v_mfma_i32_16x16x64_i8 v[62:65], v[70:73], v[176:179], v[62:65]
	v_mfma_i32_16x16x64_i8 v[54:57], v[78:81], v[176:179], v[54:57]
	v_mfma_i32_16x16x64_i8 v[46:49], v[70:73], v[194:197], v[46:49]
	v_mfma_i32_16x16x64_i8 v[38:41], v[78:81], v[194:197], v[38:41]
	v_mfma_i32_16x16x64_i8 v[30:33], v[70:73], v[202:205], v[30:33]
	v_mfma_i32_16x16x64_i8 v[22:25], v[78:81], v[202:205], v[22:25]
	v_mfma_i32_16x16x64_i8 v[14:17], v[70:73], v[210:213], v[14:17]
	v_mfma_i32_16x16x64_i8 v[6:9], v[78:81], v[210:213], v[6:9]
	v_mfma_i32_16x16x64_i8 v[62:65], v[74:77], v[180:183], v[62:65]
	v_mfma_i32_16x16x64_i8 v[54:57], v[82:85], v[180:183], v[54:57]
	v_mfma_i32_16x16x64_i8 v[46:49], v[74:77], v[198:201], v[46:49]
	v_mfma_i32_16x16x64_i8 v[38:41], v[82:85], v[198:201], v[38:41]
	v_mfma_i32_16x16x64_i8 v[30:33], v[74:77], v[206:209], v[30:33]
	v_mfma_i32_16x16x64_i8 v[22:25], v[82:85], v[206:209], v[22:25]
	v_mfma_i32_16x16x64_i8 v[14:17], v[74:77], v[214:217], v[14:17]
	v_mfma_i32_16x16x64_i8 v[6:9], v[82:85], v[214:217], v[6:9]
	s_setprio 0
	s_setprio 1
	v_mfma_i32_16x16x64_i8 v[58:61], v[94:97], v[176:179], v[58:61]
	v_mfma_i32_16x16x64_i8 v[50:53], v[102:105], v[176:179], v[50:53]
	v_mfma_i32_16x16x64_i8 v[42:45], v[94:97], v[194:197], v[42:45]
	v_mfma_i32_16x16x64_i8 v[34:37], v[102:105], v[194:197], v[34:37]
	v_mfma_i32_16x16x64_i8 v[26:29], v[94:97], v[202:205], v[26:29]
	v_mfma_i32_16x16x64_i8 v[18:21], v[102:105], v[202:205], v[18:21]
	v_mfma_i32_16x16x64_i8 v[10:13], v[94:97], v[210:213], v[10:13]
	v_mfma_i32_16x16x64_i8 v[2:5], v[102:105], v[210:213], v[2:5]
	v_mfma_i32_16x16x64_i8 v[58:61], v[98:101], v[180:183], v[58:61]
	v_mfma_i32_16x16x64_i8 v[50:53], v[106:109], v[180:183], v[50:53]
	v_mfma_i32_16x16x64_i8 v[42:45], v[98:101], v[198:201], v[42:45]
	v_mfma_i32_16x16x64_i8 v[34:37], v[106:109], v[198:201], v[34:37]
	v_mfma_i32_16x16x64_i8 v[26:29], v[98:101], v[206:209], v[26:29]
	v_mfma_i32_16x16x64_i8 v[18:21], v[106:109], v[206:209], v[18:21]
	v_mfma_i32_16x16x64_i8 v[10:13], v[98:101], v[214:217], v[10:13]
	v_mfma_i32_16x16x64_i8 v[2:5], v[106:109], v[214:217], v[2:5]
	s_setprio 0
	s_barrier
	s_add_i32 s42, 0, 0x18000
	v_add_u32_e32 v0, s42, v189
	s_add_i32 s72, 0, 0x1c000
	ds_read_b128 v[70:73], v0
	ds_read_b128 v[74:77], v0 offset:1024
	ds_read_b128 v[78:81], v0 offset:2048
	ds_read_b128 v[82:85], v0 offset:3072
	v_add_u32_e32 v0, s72, v189
	ds_read_b128 v[94:97], v0
	ds_read_b128 v[98:101], v0 offset:1024
	ds_read_b128 v[102:105], v0 offset:2048
	ds_read_b128 v[106:109], v0 offset:3072
	s_mov_b32 m0, s59
	ds_read_b128 v[176:179], v192 offset:32768
	ds_read_b128 v[180:183], v192 offset:33792
	ds_read_b128 v[194:197], v192 offset:34816
	ds_read_b128 v[198:201], v192 offset:35840
	ds_read_b128 v[202:205], v192 offset:36864
	ds_read_b128 v[206:209], v192 offset:37888
	ds_read_b128 v[210:213], v192 offset:38912
	ds_read_b128 v[214:217], v192 offset:39936
	global_load_lds_dwordx4 v187, s[48:49]
	s_mov_b32 m0, s60
	s_nop 0
	global_load_lds_dwordx4 v186, s[48:49]
	s_waitcnt vmcnt(8)
	s_waitcnt lgkmcnt(0)
	s_barrier
	s_setprio 1
	s_waitcnt lgkmcnt(0)
	v_mfma_i32_16x16x64_i8 v[158:161], v[70:73], v[176:179], v[158:161]
	v_mfma_i32_16x16x64_i8 v[150:153], v[78:81], v[176:179], v[150:153]
	v_mfma_i32_16x16x64_i8 v[142:145], v[70:73], v[194:197], v[142:145]
	v_mfma_i32_16x16x64_i8 v[134:137], v[78:81], v[194:197], v[134:137]
	v_mfma_i32_16x16x64_i8 v[126:129], v[70:73], v[202:205], v[126:129]
	v_mfma_i32_16x16x64_i8 v[118:121], v[78:81], v[202:205], v[118:121]
	v_mfma_i32_16x16x64_i8 v[110:113], v[70:73], v[210:213], v[110:113]
	v_mfma_i32_16x16x64_i8 v[86:89], v[78:81], v[210:213], v[86:89]
	v_mfma_i32_16x16x64_i8 v[158:161], v[74:77], v[180:183], v[158:161]
	v_mfma_i32_16x16x64_i8 v[150:153], v[82:85], v[180:183], v[150:153]
	v_mfma_i32_16x16x64_i8 v[142:145], v[74:77], v[198:201], v[142:145]
	v_mfma_i32_16x16x64_i8 v[134:137], v[82:85], v[198:201], v[134:137]
	v_mfma_i32_16x16x64_i8 v[126:129], v[74:77], v[206:209], v[126:129]
	v_mfma_i32_16x16x64_i8 v[118:121], v[82:85], v[206:209], v[118:121]
	v_mfma_i32_16x16x64_i8 v[110:113], v[74:77], v[214:217], v[110:113]
	v_mfma_i32_16x16x64_i8 v[86:89], v[82:85], v[214:217], v[86:89]
	s_setprio 0
	s_setprio 1
	v_mfma_i32_16x16x64_i8 v[154:157], v[94:97], v[176:179], v[154:157]
	v_mfma_i32_16x16x64_i8 v[146:149], v[102:105], v[176:179], v[146:149]
	v_mfma_i32_16x16x64_i8 v[138:141], v[94:97], v[194:197], v[138:141]
	v_mfma_i32_16x16x64_i8 v[130:133], v[102:105], v[194:197], v[130:133]
	v_mfma_i32_16x16x64_i8 v[122:125], v[94:97], v[202:205], v[122:125]
	v_mfma_i32_16x16x64_i8 v[114:117], v[102:105], v[202:205], v[114:117]
	v_mfma_i32_16x16x64_i8 v[90:93], v[94:97], v[210:213], v[90:93]
	v_mfma_i32_16x16x64_i8 v[66:69], v[102:105], v[210:213], v[66:69]
	v_mfma_i32_16x16x64_i8 v[154:157], v[98:101], v[180:183], v[154:157]
	v_mfma_i32_16x16x64_i8 v[146:149], v[106:109], v[180:183], v[146:149]
	v_mfma_i32_16x16x64_i8 v[138:141], v[98:101], v[198:201], v[138:141]
	v_mfma_i32_16x16x64_i8 v[130:133], v[106:109], v[198:201], v[130:133]
	v_mfma_i32_16x16x64_i8 v[122:125], v[98:101], v[206:209], v[122:125]
	v_mfma_i32_16x16x64_i8 v[114:117], v[106:109], v[206:209], v[114:117]
	v_mfma_i32_16x16x64_i8 v[90:93], v[98:101], v[214:217], v[90:93]
	v_mfma_i32_16x16x64_i8 v[66:69], v[106:109], v[214:217], v[66:69]
	s_setprio 0
	s_barrier
	s_add_i32 s42, s42, s57
	v_lshl_add_u64 v[184:185], v[184:185], 0, s[22:23]
	s_mov_b32 m0, s42
	s_nop 0
	global_load_lds_dwordx4 v[184:185], off
	s_add_i32 m0, s42, 0x2000
	s_add_u32 s42, s46, 0x40080
	v_lshl_add_u64 v[184:185], v[218:219], 0, s[22:23]
	s_addc_u32 s43, s47, 0
	s_add_i32 s46, s72, s57
	global_load_lds_dwordx4 v[184:185], off
	v_lshl_add_u64 v[184:185], s[42:43], 0, v[164:165]
	s_mov_b32 m0, s46
	s_nop 0
	global_load_lds_dwordx4 v[184:185], off
	v_lshl_add_u64 v[184:185], s[42:43], 0, v[166:167]
	s_add_i32 m0, s46, 0x2000
	s_nop 0
	global_load_lds_dwordx4 v[184:185], off
	v_lshl_add_u64 v[184:185], v[220:221], 0, s[22:23]
	s_mov_b32 m0, s63
	s_nop 0
	global_load_lds_dwordx4 v[184:185], off
	v_lshl_add_u64 v[184:185], v[222:223], 0, s[22:23]
	s_mov_b32 m0, s64
	s_nop 0
	global_load_lds_dwordx4 v[184:185], off
	ds_read_b128 v[176:179], v192 offset:49152
	ds_read_b128 v[180:183], v192 offset:50176
	ds_read_b128 v[194:197], v192 offset:51200
	ds_read_b128 v[198:201], v192 offset:52224
	ds_read_b128 v[202:205], v192 offset:53248
	ds_read_b128 v[206:209], v192 offset:54272
	ds_read_b128 v[210:213], v192 offset:55296
	ds_read_b128 v[214:217], v192 offset:56320
	s_waitcnt vmcnt(8)
	s_waitcnt lgkmcnt(0)
	s_barrier
	s_setprio 1
	s_waitcnt lgkmcnt(0)
	v_mfma_i32_16x16x64_i8 v[62:65], v[70:73], v[176:179], v[62:65]
	v_mfma_i32_16x16x64_i8 v[54:57], v[78:81], v[176:179], v[54:57]
	v_mfma_i32_16x16x64_i8 v[46:49], v[70:73], v[194:197], v[46:49]
	v_mfma_i32_16x16x64_i8 v[38:41], v[78:81], v[194:197], v[38:41]
	v_mfma_i32_16x16x64_i8 v[30:33], v[70:73], v[202:205], v[30:33]
	v_mfma_i32_16x16x64_i8 v[22:25], v[78:81], v[202:205], v[22:25]
	v_mfma_i32_16x16x64_i8 v[14:17], v[70:73], v[210:213], v[14:17]
	v_mfma_i32_16x16x64_i8 v[6:9], v[78:81], v[210:213], v[6:9]
	v_mfma_i32_16x16x64_i8 v[62:65], v[74:77], v[180:183], v[62:65]
	v_mfma_i32_16x16x64_i8 v[54:57], v[82:85], v[180:183], v[54:57]
	v_mfma_i32_16x16x64_i8 v[46:49], v[74:77], v[198:201], v[46:49]
	v_mfma_i32_16x16x64_i8 v[38:41], v[82:85], v[198:201], v[38:41]
	v_mfma_i32_16x16x64_i8 v[30:33], v[74:77], v[206:209], v[30:33]
	v_mfma_i32_16x16x64_i8 v[22:25], v[82:85], v[206:209], v[22:25]
	v_mfma_i32_16x16x64_i8 v[14:17], v[74:77], v[214:217], v[14:17]
	v_mfma_i32_16x16x64_i8 v[6:9], v[82:85], v[214:217], v[6:9]
	s_setprio 0
	s_setprio 1
	v_mfma_i32_16x16x64_i8 v[58:61], v[94:97], v[176:179], v[58:61]
	v_mfma_i32_16x16x64_i8 v[50:53], v[102:105], v[176:179], v[50:53]
	v_mfma_i32_16x16x64_i8 v[42:45], v[94:97], v[194:197], v[42:45]
	v_mfma_i32_16x16x64_i8 v[34:37], v[102:105], v[194:197], v[34:37]
	v_mfma_i32_16x16x64_i8 v[26:29], v[94:97], v[202:205], v[26:29]
	v_mfma_i32_16x16x64_i8 v[18:21], v[102:105], v[202:205], v[18:21]
	v_mfma_i32_16x16x64_i8 v[10:13], v[94:97], v[210:213], v[10:13]
	v_mfma_i32_16x16x64_i8 v[2:5], v[102:105], v[210:213], v[2:5]
	v_mfma_i32_16x16x64_i8 v[58:61], v[98:101], v[180:183], v[58:61]
	v_mfma_i32_16x16x64_i8 v[50:53], v[106:109], v[180:183], v[50:53]
	v_mfma_i32_16x16x64_i8 v[42:45], v[98:101], v[198:201], v[42:45]
	v_mfma_i32_16x16x64_i8 v[34:37], v[106:109], v[198:201], v[34:37]
	v_mfma_i32_16x16x64_i8 v[26:29], v[98:101], v[206:209], v[26:29]
	v_mfma_i32_16x16x64_i8 v[18:21], v[106:109], v[206:209], v[18:21]
	v_mfma_i32_16x16x64_i8 v[10:13], v[98:101], v[214:217], v[10:13]
	v_mfma_i32_16x16x64_i8 v[2:5], v[106:109], v[214:217], v[2:5]
	s_setprio 0
	s_barrier
	s_add_i32 s39, s39, 2
	s_cmp_gt_u32 s39, 13
	s_mov_b64 s[42:43], s[44:45]
	s_cbranch_scc0 .LBB0_1214

.LBB0_1239:
	s_waitcnt vmcnt(0)
	s_barrier
	s_mov_b64 s[0:1], exec
	v_readlane_b32 s4, v252, 11
	v_readlane_b32 s5, v252, 12
	s_and_b64 s[4:5], s[0:1], s[4:5]
	s_mov_b64 exec, s[4:5]
	s_cbranch_execz .LBB0_1291
	s_add_i32 s4, 0, 0x26f20
	v_mov_b32_e32 v0, s4
	s_waitcnt vmcnt(0) expcnt(0) lgkmcnt(0)
	ds_read_b32 v3, v0
	s_add_i32 s4, 0, 0x26f24
	v_mov_b32_e32 v0, s4
	ds_read_b32 v1, v0
	s_waitcnt lgkmcnt(1)
	v_cmp_ne_u32_e32 vcc, 0, v3
	s_cbranch_vccnz .LBB0_1255
	v_readlane_b32 s4, v252, 4
	v_readlane_b32 s5, v252, 5
	s_load_dwordx2 s[10:11], s[4:5], 0x4
	v_readlane_b32 s42, v252, 2
	v_readlane_b32 s43, v252, 3
	s_add_u32 s4, s42, 0x4200
	s_addc_u32 s5, s43, 0
	s_add_u32 s6, s42, 0x4400
	s_addc_u32 s7, s43, 0
	v_readlane_b32 s14, v252, 6
	s_waitcnt lgkmcnt(0)
	s_mul_i32 s51, s10, s14
	s_add_u32 s10, s42, 0x4500
	s_mul_i32 s51, s51, s11
	s_addc_u32 s11, s43, 0
	v_readlane_b32 s15, v252, 7
	s_add_u32 s14, s42, 0x4600
	s_addc_u32 s15, s43, 0
	s_add_u32 s16, s42, 0x4700
	s_addc_u32 s17, s43, 0
	s_add_u32 s18, s42, 0x4800
	s_addc_u32 s19, s43, 0
	s_add_u32 s20, s42, 0x4900
	s_addc_u32 s21, s43, 0
	s_add_u32 s22, s42, 0x4a00
	s_addc_u32 s23, s43, 0
	s_add_u32 s24, s42, 0x4b00
	s_addc_u32 s25, s43, 0
	s_add_u32 s26, s42, 0x4c00
	s_addc_u32 s27, s43, 0
	s_add_u32 s28, s42, 0x4d00
	s_addc_u32 s29, s43, 0
	s_add_u32 s30, s42, 0x4e00
	s_addc_u32 s31, s43, 0
	s_add_u32 s34, s42, 0x4f00
	s_addc_u32 s35, s43, 0
	s_add_u32 s36, s42, 0x5000
	s_addc_u32 s37, s43, 0
	s_add_u32 s38, s42, 0x5100
	s_addc_u32 s39, s43, 0
	s_add_u32 s40, s42, 0x5200
	s_addc_u32 s41, s43, 0
	s_add_u32 s42, s42, 0x5300
	s_addc_u32 s43, s43, 0
	s_mov_b32 s52, 1
	v_mov_b32_e32 v17, 0
	s_branch .LBB0_1243
	s_nop 0
	s_nop 0
	s_nop 0
	s_nop 0
	s_nop 0
	s_nop 0
	s_nop 0
	s_nop 0
	s_nop 0
	s_nop 0
	s_nop 0
	s_nop 0
	s_nop 0
	s_nop 0
	s_nop 0
	s_nop 0
	s_nop 0
	s_nop 0
	s_nop 0
	s_nop 0
	s_nop 0
	s_nop 0
	s_nop 0
	s_nop 0
	s_nop 0
	s_nop 0
	s_nop 0
	s_nop 0
	s_nop 0
	s_nop 0
	s_nop 0
	s_nop 0
	s_nop 0
	s_nop 0
	s_nop 0
	s_nop 0
	s_nop 0
	s_nop 0
	s_nop 0
	s_nop 0
	s_nop 0
	s_nop 0
	s_nop 0
	s_nop 0
	s_nop 0
	s_nop 0
